# v28 + FOX unit prologue: next-ticket atomic without a wait at unit start; tile-skip F loads issued beside the gain loads (one round trip less)
# speedup vs baseline: 1.0058x; 1.0058x over previous
; template <class CV>
; __device__ __forceinline__ void attn_phase(const Args& A, int vcu, int G, LAS char* shm, int repm, int repf, LAS float* dg, unsigned* qctr, const float* bfox, LAS int* qs  , int nscan, int ncv, CV cv) {
;     ...
;         const int idx = qs[8];
;         if (idx >= 1024 * repf + ncv) break;
;         const int g4 = idx >> 1; const bool isc = ((idx & 1) == 1) && g4 < ncv;
;         const int id = (idx - (g4 < ncv ? g4 : ncv)) & 1023, h = qs[id >> 7], rem = id & 127, qb = 31 - (rem >> 2), b = rem & 3;
;         unsigned nxt = 0u;
;         __syncthreads();
;         if (tid == 0) nxt = __hip_atomic_fetch_add(qctr, 1u, __ATOMIC_RELAXED, __HIP_MEMORY_SCOPE_AGENT);
.LBB0_922:
	s_ashr_i32 s2, s3, 1
	s_min_i32 s0, s2, s74
	s_sub_i32 s1, s3, s0
	s_lshr_b32 s0, s1, 5
	s_and_b32 s0, s0, 28
	s_add_i32 s0, s71, s0
	v_mov_b32_e32 v1, s0
	ds_read_b32 v1, v1
	s_waitcnt lgkmcnt(0)
	s_barrier
	v_readfirstlane_b32 s0, v1
	v_mov_b32_e32 v1, 0
	s_mov_b64 s[12:13], exec
	v_readlane_b32 s4, v253, 22
	v_readlane_b32 s5, v253, 23
	s_and_b64 s[4:5], s[12:13], s[4:5]
	s_mov_b64 exec, s[4:5]
	s_cbranch_execz .LBB0_926
	s_mov_b64 s[18:19], exec
	v_mbcnt_lo_u32_b32 v1, s18, 0
	v_mbcnt_hi_u32_b32 v1, s19, v1
	v_cmp_eq_u32_e32 vcc, 0, v1
	s_and_saveexec_b64 s[14:15], vcc
	s_cbranch_execz .LBB0_925
	s_bcnt1_i32_b64 s4, s[18:19]
	v_mov_b32_e32 v1, s4
	global_atomic_add v1, v131, v1, s[28:29] sc0

; template <bool FOX>
; __device__ __forceinline__ void attn_unit(const Args& A, int b, int h, int qb, LAS char* shm, LAS float* dg) {
;     ...
;         float gq = fmaxf(fabsf(A.gfq[lane]), 0.f), gk = fabsf(A.gfk[lane]);
; #pragma unroll
;         for (int o = 32; o > 0; o >>= 1) { gq = fmaxf(gq, __shfl_xor(gq, o)); gk = fmaxf(gk, __shfl_xor(gk, o)); }
;         const float margin = 2.f * (8.f * gq * gk) + SKIP_NATS;
;         const float Fref = A.F[(rowbase + q0) * 8 + h];
;         const int nfull = q0 / 64;
;         bool keep0 = true, keep1 = true;
;         if (lane < nfull) keep0 = (Fref - A.F[(rowbase + 64 * lane + 63) * 8 + h]) >= -margin;
;         if (lane + 64 < nfull) keep1 = (Fref - A.F[(rowbase + 64 * (lane + 64) + 63) * 8 + h]) >= -margin;
;         const unsigned long long k0 = __ballot(keep0), k1 = __ballot(keep1);
;         t0 = k0 ? __builtin_ctzll(k0) : 64 + (k1 ? __builtin_ctzll(k1) : 0);
.LBB0_926:
	s_or_b64 exec, exec, s[12:13]
	s_bitcmp0_b32 s3, 0
	s_cselect_b64 s[4:5], -1, 0
	s_cmp_ge_i32 s2, s74
	s_cselect_b64 s[6:7], -1, 0
	s_or_b64 s[4:5], s[4:5], s[6:7]
	s_mov_b64 s[12:13], -1
	s_and_b64 vcc, exec, s[4:5]
	s_cbranch_vccz .LBB0_1017
	v_mov_b32_e32 v128, v0
	v_and_b32_e32 v6, 64, v237
	v_and_b32_e32 v191, 63, v128
	v_lshlrev_b32_e32 v3, 2, v191
	global_load_dword v4, v3, s[36:37]
	v_add_u32_e32 v6, 64, v6
	global_load_dword v3, v3, s[88:89]
	v_xor_b32_e32 v7, 32, v237
	v_cmp_lt_i32_e32 vcc, v7, v6
	s_not_b32 s3, s1
	s_bfe_u32 s3, s3, 0x50002
	v_cndmask_b32_e32 v7, v237, v7, vcc
	v_lshlrev_b32_e32 v7, 2, v7
	s_and_b32 s4, s1, 3
	s_lshl_b32 s6, s4, 13
	s_lshl_b32 s5, s3, 8
	s_or_b32 s8, s5, s6
	s_ashr_i32 s1, s0, 31
	s_lshl_b32 s8, s8, 5
	s_add_u32 s8, s34, s8
	s_addc_u32 s15, s35, 0
	s_lshl_b64 s[12:13], s[0:1], 2
	s_add_u32 s14, s8, s12
	s_addc_u32 s15, s15, s13
	s_lshl_b32 s3, s3, 2
	v_readfirstlane_b32 s7, v128
	s_mov_b64 s[18:19], -1
	global_load_dword v20, v131, s[14:15]
	s_lshl_b32 s8, s4, 18
	v_lshl_or_b32 v130, v191, 11, s8
	s_mov_b64 s[22:23], 0x20000
	v_lshl_add_u64 v[10:11], s[34:35], 0, v[130:131]
	v_lshl_add_u64 v[10:11], s[0:1], 2, v[10:11]
	global_load_dword v21, v[10:11], off offset:2016
	v_lshl_add_u64 v[12:13], v[10:11], 0, s[22:23]
	global_load_dword v22, v[12:13], off offset:2016
	s_waitcnt vmcnt(4)
	v_max_f32_e64 v4, |v4|, |v4|
	v_max_f32_e32 v4, 0, v4
	s_waitcnt vmcnt(3)
	v_and_b32_e32 v5, 0x7fffffff, v3
	ds_bpermute_b32 v5, v7, v5
	ds_bpermute_b32 v8, v7, v4
	v_max_f32_e64 v3, |v3|, |v3|
	s_waitcnt lgkmcnt(1)
	v_max_f32_e32 v5, v5, v5
	v_max_f32_e32 v3, v3, v5
	v_xor_b32_e32 v5, 16, v237
	v_cmp_lt_i32_e32 vcc, v5, v6
	s_waitcnt lgkmcnt(0)
	v_max_f32_e32 v8, v8, v8
	v_max_f32_e32 v4, v4, v8
	v_cndmask_b32_e32 v5, v237, v5, vcc
	v_lshlrev_b32_e32 v5, 2, v5
	ds_bpermute_b32 v7, v5, v4
	ds_bpermute_b32 v5, v5, v3
	s_waitcnt lgkmcnt(1)
	v_max_f32_e32 v7, v7, v7
	s_waitcnt lgkmcnt(0)
	v_max_f32_e32 v5, v5, v5
	v_max_f32_e32 v3, v3, v5
	v_xor_b32_e32 v5, 8, v237
	v_cmp_lt_i32_e32 vcc, v5, v6
	v_max_f32_e32 v4, v4, v7
	s_nop 0
	v_cndmask_b32_e32 v5, v237, v5, vcc
	v_lshlrev_b32_e32 v5, 2, v5
	ds_bpermute_b32 v7, v5, v4
	ds_bpermute_b32 v5, v5, v3
	s_waitcnt lgkmcnt(1)
	v_max_f32_e32 v7, v7, v7
	s_waitcnt lgkmcnt(0)
	v_max_f32_e32 v5, v5, v5
	v_max_f32_e32 v5, v3, v5
	v_xor_b32_e32 v3, 4, v237
	v_cmp_lt_i32_e32 vcc, v3, v6
	v_max_f32_e32 v4, v4, v7
	s_nop 0
	v_cndmask_b32_e32 v3, v237, v3, vcc
	v_lshlrev_b32_e32 v3, 2, v3
	ds_bpermute_b32 v7, v3, v4
	s_waitcnt lgkmcnt(0)
	v_max_f32_e32 v7, v7, v7
	v_max_f32_e32 v4, v4, v7
	ds_bpermute_b32 v7, v3, v5
	s_waitcnt lgkmcnt(0)
	v_max_f32_e32 v7, v7, v7
	v_max_f32_e32 v5, v5, v7
	v_xor_b32_e32 v7, 2, v237
	v_cmp_lt_i32_e32 vcc, v7, v6
	s_nop 1
	v_cndmask_b32_e32 v7, v237, v7, vcc
	v_lshlrev_b32_e32 v134, 2, v7
	ds_bpermute_b32 v7, v134, v4
	s_waitcnt lgkmcnt(0)
	v_max_f32_e32 v7, v7, v7
	v_max_f32_e32 v4, v4, v7
	ds_bpermute_b32 v7, v134, v5
	s_waitcnt lgkmcnt(0)
	v_max_f32_e32 v7, v7, v7
	v_max_f32_e32 v5, v5, v7
	v_xor_b32_e32 v7, 1, v237
	v_cmp_lt_i32_e32 vcc, v7, v6
	s_nop 1
	v_cndmask_b32_e32 v6, v237, v7, vcc
	v_lshlrev_b32_e32 v190, 2, v6
	ds_bpermute_b32 v6, v190, v4
	v_cmp_gt_u32_e32 vcc, s3, v191
	s_waitcnt lgkmcnt(0)
	v_max_f32_e32 v6, v6, v6
	v_max_f32_e32 v4, v4, v6
	ds_bpermute_b32 v6, v190, v5
	v_mul_f32_e32 v4, 0x41000000, v4
	s_waitcnt lgkmcnt(0)
	v_max_f32_e32 v6, v6, v6
	v_max_f32_e32 v5, v5, v6
	v_mul_f32_e32 v4, v5, v4
	v_mul_f32_e32 v240, 0x3fb8aa3b, v4
	v_fmaak_f32 v5, 2.0, v4, 0x42000000
	s_waitcnt vmcnt(0)
	v_mov_b32_e32 v4, v20
	s_mov_b64 s[14:15], -1
	s_and_saveexec_b64 s[22:23], vcc
	s_cbranch_execz .LBB0_929
	v_sub_f32_e32 v6, v4, v21
	v_cmp_ge_f32_e64 s[18:19], v6, -v5
	s_orn2_b64 s[18:19], s[18:19], exec
.LBB0_929:
	s_or_b64 exec, exec, s[22:23]
	v_or_b32_e32 v6, 64, v191
	v_cmp_gt_u32_e32 vcc, s3, v6
	s_and_saveexec_b64 s[22:23], vcc
	s_cbranch_execz .LBB0_931
	v_sub_f32_e32 v6, v4, v22
	v_cmp_ge_f32_e64 s[14:15], v6, -v5
	s_orn2_b64 s[14:15], s[14:15], exec

; template <class CV>
; __device__ __forceinline__ void attn_phase(const Args& A, int vcu, int G, LAS char* shm, int repm, int repf, LAS float* dg, unsigned* qctr, const float* bfox, LAS int* qs  , int nscan, int ncv, CV cv) {
;     ...
;         if (tid == 0) qs[8] = (int)nxt;
;         asm volatile("s_waitcnt vmcnt(0) lgkmcnt(0)" ::: "memory"); __syncthreads();
.LBB0_1540:
	s_mov_b64 s[0:1], exec
	v_readlane_b32 s2, v253, 22
	v_readlane_b32 s3, v253, 23
	s_and_b64 s[2:3], s[0:1], s[2:3]
	s_mov_b64 exec, s[2:3]
	s_cbranch_execz .LBB0_921
	s_waitcnt vmcnt(0) lgkmcnt(0)
	v_mov_b32_e32 v3, s75
	ds_write_b32 v3, v1
	s_branch .LBB0_921
